# speedup vs baseline: 1.0196x; 1.0196x over previous
.Lk1_nbx7:
.Lk1_nb_done:
	s_lshl_b32 s32, s24, 6
	s_add_u32 s40, s12, s32
	s_addc_u32 s41, s13, 0
	s_lshl_b32 s32, s24, 4
	s_add_u32 s42, s14, s32
	s_addc_u32 s43, s15, 0
	v_lshlrev_b32_e32 v47, 3, v1
	v_lshlrev_b32_e32 v48, 1, v1
	s_mov_b64 exec, 0xff
	global_store_dwordx2 v47, v[44:45], s[40:41]
	global_store_short v48, v46, s[42:43]
	s_mov_b64 exec, -1
	s_load_dwordx4 s[8:11], s[0:1], 0x18
	s_load_dwordx2 s[12:13], s[0:1], 0x28
	s_load_dwordx4 s[16:19], s[0:1], 0x40
	s_mov_b32 s40, 0x652b82fe
	s_mov_b32 s41, 0x3ff71547
	s_mov_b32 s42, 0xfee00000
	s_mov_b32 s43, 0xbfe62e42
	s_mov_b32 s44, 0x35793c76
	s_mov_b32 s45, 0xbdea39ef
	s_mov_b32 s46, 0xb7789f5c
	s_mov_b32 s47, 0x3e927e4f
	s_mov_b32 s48, 0xa556c734
	s_mov_b32 s49, 0x3ec71de3
	s_mov_b32 s50, 0x1a01a01a
	s_mov_b32 s51, 0x3efa01a0
	s_mov_b32 s52, 0x1a01a01a
	s_mov_b32 s53, 0x3f2a01a0
	s_mov_b32 s54, 0x16c16c17
	s_mov_b32 s55, 0x3f56c16c
	s_mov_b32 s56, 0x11111111
	s_mov_b32 s57, 0x3f811111
	s_mov_b32 s58, 0x55555555
	s_mov_b32 s59, 0x3fa55555
	s_mov_b32 s60, 0x55555555
	s_mov_b32 s61, 0x3fc55555
	v_mov_b32_e32 v44, 0x67f544e4
	v_mov_b32_e32 v45, 0x3e5ae645
	s_mov_b32 s62, 0xfefa39ef
	s_mov_b32 s63, 0x3fe62e42
	s_waitcnt vmcnt(2)
	v_readlane_b32 s64, v16, 0
	v_readlane_b32 s65, v17, 0
	v_readlane_b32 s66, v18, 0
	v_readlane_b32 s67, v19, 0
	s_cmp_eq_u32 s35, 1
	s_cselect_b32 s64, s65, s64
	s_cmp_eq_u32 s35, 2
	s_cselect_b32 s64, s66, s64
	s_cmp_eq_u32 s35, 3
	s_cselect_b32 s36, s67, s64
	s_cmp_le_u32 0, s35
	s_cselect_b64 s[32:33], 1, 0
	v_cndmask_b32_e64 v16, v16, v15, s[32:33]
	s_cmp_le_u32 1, s35
	s_cselect_b64 s[32:33], 1, 0
	v_cndmask_b32_e64 v17, v17, v15, s[32:33]
	s_cmp_le_u32 2, s35
	s_cselect_b64 s[32:33], 1, 0
	v_cndmask_b32_e64 v18, v18, v15, s[32:33]
	s_cmp_le_u32 3, s35
	s_cselect_b64 s[32:33], 1, 0
	v_cndmask_b32_e64 v19, v19, v15, s[32:33]
	s_cmp_lt_u32 s35, 1
	s_cselect_b64 s[32:33], 0x10000, 0
	v_cndmask_b32_e64 v41, v41, v15, s[32:33]
	s_cmp_lt_u32 s35, 2
	s_cselect_b64 s[32:33], 0x10000, 0
	v_cndmask_b32_e64 v42, v42, v15, s[32:33]
	s_cmp_lt_u32 s35, 3
	s_cselect_b64 s[32:33], 0x10000, 0
	v_cndmask_b32_e64 v43, v43, v15, s[32:33]
	v_max3_f32 v52, v16, v17, v18
	v_max3_f32 v53, v19, v20, v21
	v_max3_f32 v52, v52, v22, v23
	v_max3_f32 v53, v53, v24, v25
	v_max3_f32 v52, v52, v26, v27
	v_max3_f32 v52, v52, v28, v29
	v_max3_f32 v53, v53, v30, v31
	v_max3_f32 v52, v52, v32, v33
	v_max3_f32 v52, v52, v34, v35
	v_max3_f32 v53, v53, v36, v37
	v_max3_f32 v52, v52, v38, v39
	v_max3_f32 v53, v53, v40, v41
	v_max3_f32 v52, v52, v42, v43
	v_max_f32_e32 v52, v52, v53
	s_nop 1
	v_max_f32_dpp v52, v52, v52 quad_perm:[1,0,3,2] row_mask:0xf bank_mask:0xf
	s_nop 1
	v_max_f32_dpp v52, v52, v52 quad_perm:[2,3,0,1] row_mask:0xf bank_mask:0xf
	s_nop 1
	v_max_f32_dpp v52, v52, v52 row_half_mirror row_mask:0xf bank_mask:0xf
	s_nop 1
	v_max_f32_dpp v52, v52, v52 row_mirror row_mask:0xf bank_mask:0xf
	s_nop 1
	v_max_f32_dpp v52, v52, v52 row_bcast:15 row_mask:0xa bank_mask:0xf
	s_nop 1
	v_max_f32_dpp v52, v52, v52 row_bcast:31 row_mask:0xc bank_mask:0xf
	s_nop 1
	v_readlane_b32 s28, v52, 63
	v_mov_b32_e32 v53, s36
	v_mov_b32_e32 v56, 0x3fb8aa3b
	v_mov_b32_e32 v57, 0x3fb8aa3b
	v_max_f32_e32 v53, s28, v53
	v_mul_f32_e32 v58, 0xbfb8aa3b, v53
	v_mov_b32_e32 v6, 0
	v_mov_b32_e32 v7, 0
	v_mov_b32_e32 v59, v58
	v_pk_fma_f32 v[60:61], v[16:17], v[56:57], v[58:59]
	v_pk_fma_f32 v[62:63], v[18:19], v[56:57], v[58:59]
	v_exp_f32_e32 v60, v60
	v_exp_f32_e32 v61, v61
	v_exp_f32_e32 v62, v62
	v_exp_f32_e32 v63, v63
	s_nop 0
	v_pk_add_f32 v[60:61], v[60:61], v[62:63]
	s_nop 0
	v_add_f32_e32 v60, v60, v61
	v_cvt_f64_f32_e32 v[4:5], v60
	v_add_f64 v[6:7], v[6:7], v[4:5]
	v_pk_fma_f32 v[60:61], v[20:21], v[56:57], v[58:59]
	v_pk_fma_f32 v[62:63], v[22:23], v[56:57], v[58:59]
	v_exp_f32_e32 v60, v60
	v_exp_f32_e32 v61, v61
	v_exp_f32_e32 v62, v62
	v_exp_f32_e32 v63, v63
	s_nop 0
	v_pk_add_f32 v[60:61], v[60:61], v[62:63]
	s_nop 0
	v_add_f32_e32 v60, v60, v61
	v_cvt_f64_f32_e32 v[4:5], v60
	v_add_f64 v[6:7], v[6:7], v[4:5]
	v_pk_fma_f32 v[60:61], v[24:25], v[56:57], v[58:59]
	v_pk_fma_f32 v[62:63], v[26:27], v[56:57], v[58:59]
	v_exp_f32_e32 v60, v60
	v_exp_f32_e32 v61, v61
	v_exp_f32_e32 v62, v62
	v_exp_f32_e32 v63, v63
	s_nop 0
	v_pk_add_f32 v[60:61], v[60:61], v[62:63]
	s_nop 0
	v_add_f32_e32 v60, v60, v61
	v_cvt_f64_f32_e32 v[4:5], v60
	v_add_f64 v[6:7], v[6:7], v[4:5]
	v_pk_fma_f32 v[60:61], v[28:29], v[56:57], v[58:59]
	v_pk_fma_f32 v[62:63], v[30:31], v[56:57], v[58:59]
	v_exp_f32_e32 v60, v60
	v_exp_f32_e32 v61, v61
	v_exp_f32_e32 v62, v62
	v_exp_f32_e32 v63, v63
	s_nop 0
	v_pk_add_f32 v[60:61], v[60:61], v[62:63]
	s_nop 0
	v_add_f32_e32 v60, v60, v61
	v_cvt_f64_f32_e32 v[4:5], v60
	v_add_f64 v[6:7], v[6:7], v[4:5]
	v_pk_fma_f32 v[60:61], v[32:33], v[56:57], v[58:59]
	v_pk_fma_f32 v[62:63], v[34:35], v[56:57], v[58:59]
	v_exp_f32_e32 v60, v60
	v_exp_f32_e32 v61, v61
	v_exp_f32_e32 v62, v62
	v_exp_f32_e32 v63, v63
	s_nop 0
	v_pk_add_f32 v[60:61], v[60:61], v[62:63]
	s_nop 0
	v_add_f32_e32 v60, v60, v61
	v_cvt_f64_f32_e32 v[4:5], v60
	v_add_f64 v[6:7], v[6:7], v[4:5]
	v_pk_fma_f32 v[60:61], v[36:37], v[56:57], v[58:59]
	v_pk_fma_f32 v[62:63], v[38:39], v[56:57], v[58:59]
	v_exp_f32_e32 v60, v60
	v_exp_f32_e32 v61, v61
	v_exp_f32_e32 v62, v62
	v_exp_f32_e32 v63, v63
	s_nop 0
	v_pk_add_f32 v[60:61], v[60:61], v[62:63]
	s_nop 0
	v_add_f32_e32 v60, v60, v61
	v_cvt_f64_f32_e32 v[4:5], v60
	v_add_f64 v[6:7], v[6:7], v[4:5]
	v_pk_fma_f32 v[60:61], v[40:41], v[56:57], v[58:59]
	v_pk_fma_f32 v[62:63], v[42:43], v[56:57], v[58:59]
	v_exp_f32_e32 v60, v60
	v_exp_f32_e32 v61, v61
	v_exp_f32_e32 v62, v62
	v_exp_f32_e32 v63, v63
	s_nop 0
	v_pk_add_f32 v[60:61], v[60:61], v[62:63]
	s_nop 0
	v_add_f32_e32 v60, v60, v61
	v_cvt_f64_f32_e32 v[4:5], v60
	v_add_f64 v[6:7], v[6:7], v[4:5]
	v_mov_b32_e32 v60, s36
	v_fmamk_f32 v60, v60, 0x3fb8aa3b, v58
	v_exp_f32_e32 v60, v60
	s_nop 1
	v_mov_b32_dpp v4, v6 quad_perm:[1,0,3,2] row_mask:0xf bank_mask:0xf
	v_mov_b32_dpp v5, v7 quad_perm:[1,0,3,2] row_mask:0xf bank_mask:0xf
	v_add_f64 v[6:7], v[6:7], v[4:5]
	s_nop 1
	v_mov_b32_dpp v4, v6 quad_perm:[2,3,0,1] row_mask:0xf bank_mask:0xf
	v_mov_b32_dpp v5, v7 quad_perm:[2,3,0,1] row_mask:0xf bank_mask:0xf
	v_add_f64 v[6:7], v[6:7], v[4:5]
	s_nop 1
	v_mov_b32_dpp v4, v6 row_half_mirror row_mask:0xf bank_mask:0xf
	v_mov_b32_dpp v5, v7 row_half_mirror row_mask:0xf bank_mask:0xf
	v_add_f64 v[6:7], v[6:7], v[4:5]
	s_nop 1
	v_mov_b32_dpp v4, v6 row_mirror row_mask:0xf bank_mask:0xf
	v_mov_b32_dpp v5, v7 row_mirror row_mask:0xf bank_mask:0xf
	v_add_f64 v[6:7], v[6:7], v[4:5]
	v_cvt_f64_f32_e32 v[8:9], v60
	v_readlane_b32 s64, v6, 15
	v_readlane_b32 s65, v7, 15
	v_readlane_b32 s66, v6, 31
	v_readlane_b32 s67, v7, 31
	v_readlane_b32 s68, v6, 47
	v_readlane_b32 s69, v7, 47
	v_readlane_b32 s70, v6, 63
	v_readlane_b32 s71, v7, 63
	v_add_f64 v[6:7], s[64:65], 0
	v_add_f64 v[6:7], v[6:7], s[66:67]
	v_add_f64 v[6:7], v[6:7], s[68:69]
	v_add_f64 v[6:7], v[6:7], s[70:71]
	v_add_f64 v[6:7], v[6:7], v[8:9]
	s_mov_b32 s29, 1
	s_mov_b32 s31, 1
	s_mov_b32 s30, 0xff800000
	s_cmp_eq_u32 s27, 0
	s_cbranch_scc1 .Lk1_lse
	s_mov_b32 s37, 0x7fffffff
	v_cmp_eq_f32_e64 s[64:65], s28, v16
	v_cmp_eq_f32_e64 s[66:67], s28, v17
	v_cmp_eq_f32_e64 s[68:69], s28, v18
	v_cmp_eq_f32_e64 s[70:71], s28, v19
	s_or_b64 s[32:33], s[64:65], s[66:67]
	s_or_b64 s[72:73], s[68:69], s[70:71]
	s_or_b64 s[32:33], s[32:33], s[72:73]
	s_cmp_eq_u64 s[32:33], 0
	s_cbranch_scc1 .Lk1_a1_n0
	s_ff1_i32_b64 s32, s[64:65]
	s_lshl_b32 s33, s32, 2
	s_cmp_lt_i32 s32, 0
	s_cselect_b32 s33, 0x7fffffff, s33
	s_min_u32 s37, s37, s33
	s_ff1_i32_b64 s32, s[66:67]
	s_lshl_b32 s33, s32, 2
	s_add_u32 s33, s33, 1
	s_cmp_lt_i32 s32, 0
	s_cselect_b32 s33, 0x7fffffff, s33
	s_min_u32 s37, s37, s33
	s_ff1_i32_b64 s32, s[68:69]
	s_lshl_b32 s33, s32, 2
	s_add_u32 s33, s33, 2
	s_cmp_lt_i32 s32, 0
	s_cselect_b32 s33, 0x7fffffff, s33
	s_min_u32 s37, s37, s33
	s_ff1_i32_b64 s32, s[70:71]
	s_lshl_b32 s33, s32, 2
	s_add_u32 s33, s33, 3
	s_cmp_lt_i32 s32, 0
	s_cselect_b32 s33, 0x7fffffff, s33
	s_min_u32 s37, s37, s33
	s_lshr_b32 s32, s37, 2
	s_and_b32 s33, s37, 3
	s_lshl_b64 s[72:73], 1, s32
	s_cmp_eq_u32 s33, 0
	s_cselect_b64 s[64:65], s[72:73], 0
	v_cndmask_b32_e64 v16, v16, v15, s[64:65]
	s_cmp_eq_u32 s33, 1
	s_cselect_b64 s[64:65], s[72:73], 0
	v_cndmask_b32_e64 v17, v17, v15, s[64:65]
	s_cmp_eq_u32 s33, 2
	s_cselect_b64 s[64:65], s[72:73], 0
	v_cndmask_b32_e64 v18, v18, v15, s[64:65]
	s_cmp_eq_u32 s33, 3
	s_cselect_b64 s[64:65], s[72:73], 0
	v_cndmask_b32_e64 v19, v19, v15, s[64:65]
	s_sub_u32 s37, s37, s35
	s_branch .Lk1_a1_done

.Lk1_lse:
	v_cvt_f32_f64_e32 v52, v[6:7]
	v_log_f32_e32 v52, v52
	s_nop 0
	v_mul_f32_e32 v52, 0x3f317218, v52
	v_cvt_f64_f32_e32 v[8:9], v52
	v_mul_f64 v[10:11], v[8:9], -1.0
	v_mul_f64 v[46:47], v[10:11], s[40:41]
	v_rndne_f64_e32 v[46:47], v[46:47]
	v_fma_f64 v[10:11], v[46:47], s[42:43], v[10:11]
	v_fma_f64 v[10:11], v[46:47], s[44:45], v[10:11]
	v_fma_f64 v[48:49], v[44:45], v[10:11], s[46:47]
	v_fma_f64 v[48:49], v[48:49], v[10:11], s[48:49]
	v_fma_f64 v[48:49], v[48:49], v[10:11], s[50:51]
	v_fma_f64 v[48:49], v[48:49], v[10:11], s[52:53]
	v_fma_f64 v[48:49], v[48:49], v[10:11], s[54:55]
	v_fma_f64 v[48:49], v[48:49], v[10:11], s[56:57]
	v_fma_f64 v[48:49], v[48:49], v[10:11], s[58:59]
	v_fma_f64 v[48:49], v[48:49], v[10:11], s[60:61]
	v_fma_f64 v[48:49], v[48:49], v[10:11], 0.5
	v_fma_f64 v[48:49], v[48:49], v[10:11], 1.0
	v_fma_f64 v[48:49], v[48:49], v[10:11], 1.0
	v_cvt_i32_f64_e32 v50, v[46:47]
	v_ldexp_f64 v[48:49], v[48:49], v50
	v_fma_f64 v[48:49], v[6:7], v[48:49], -1.0
	v_add_f64 v[8:9], v[8:9], v[48:49]
	v_cvt_f64_f32_e32 v[10:11], v58
	v_fma_f64 v[8:9], -v[10:11], s[62:63], v[8:9]
	s_lshl_b32 s32, s24, 3
	s_lshl_b32 s33, s24, 2
	v_mov_b32_e32 v4, s28
	v_mov_b32_e32 v5, s29
	v_mov_b32_e32 v6, s30
	v_mov_b32_e32 v7, s31
	v_mov_b32_e32 v10, s32
	v_mov_b32_e32 v11, s33
	s_mov_b64 exec, 1
	s_waitcnt lgkmcnt(0)
	global_store_dwordx2 v10, v[8:9], s[8:9]
	global_store_dword v11, v4, s[10:11]
	global_store_dword v11, v5, s[12:13]
	global_store_dword v11, v6, s[16:17]
	global_store_dword v11, v7, s[18:19]
	s_endpgm
